# baseline (speedup 1.0000x reference)
_Z11gemm_kernelILi256ELi192ELi4ELi2ELi4ELi2ELi2ELi0EEvPKDF16_S1_iiiPDF16_PfPK15HIP_vector_typeIfLj2EE:
	s_load_dwordx8 s[4:11], s[0:1], 0x0
	s_load_dwordx2 s[12:13], s[0:1], 0x30
	s_lshr_b32 s18, s2, 3
	v_readfirstlane_b32 s17, v0
	s_lshr_b32 s14, s17, 6
	s_waitcnt lgkmcnt(0)
	s_ashr_i32 s11, s8, 31
	s_lshr_b32 s3, s11, 22
	s_add_i32 s3, s8, s3
	s_ashr_i32 s15, s3, 10
	s_abs_i32 s16, s15
	v_cvt_f32_u32_e32 v1, s16
	s_sub_i32 s21, 0, s16
	s_mul_hi_i32 s19, s9, 0x2aaaaaab
	s_lshr_b32 s20, s19, 31
	v_rcp_iflag_f32_e32 v1, v1
	s_ashr_i32 s19, s19, 6
	s_add_i32 s19, s19, s20
	s_bfe_u32 s20, s2, 0x20001
	v_mul_f32_e32 v1, 0x4f7ffffe, v1
	v_cvt_u32_f32_e32 v1, v1
	s_ashr_i32 s3, s3, 31
	s_mul_i32 s20, s15, s20
	v_mov_b32_e32 v97, 0
	v_readfirstlane_b32 s22, v1
	s_mul_i32 s21, s21, s22
	s_mul_hi_u32 s21, s22, s21
	s_add_i32 s22, s22, s21
	s_mul_hi_u32 s22, s18, s22
	s_mul_i32 s21, s22, s16
	s_sub_i32 s23, s18, s21
	s_add_i32 s24, s22, 1
	s_sub_i32 s25, s23, s16
	s_cmp_ge_u32 s23, s16
	s_cselect_b32 s22, s24, s22
	s_cselect_b32 s23, s25, s23
	s_add_i32 s24, s22, 1
	s_cmp_ge_u32 s23, s16
	s_cselect_b32 s16, s24, s22
	s_xor_b32 s16, s16, s3
	s_sub_i32 s3, s16, s3
	s_mul_i32 s15, s3, s15
	s_sub_i32 s15, s18, s15
	s_add_i32 s15, s15, s20
	s_bitcmp1_b32 s2, 0
	v_bfe_u32 v1, v0, 3, 3
	s_cselect_b32 s2, s19, 0
	v_lshl_or_b32 v1, s14, 3, v1
	s_add_i32 s18, s3, s2
	s_lshl_b32 s19, s15, 8
	v_lshrrev_b32_e32 v2, 1, v1
	s_lshl_b32 s2, s14, 10
	v_xor_b32_e32 v6, v2, v0
	v_add_u32_e32 v2, s19, v1
	s_cmp_lg_u32 0, -1
	s_mul_i32 s15, s18, 0xc0
	v_ashrrev_i32_e32 v3, 31, v2
	s_cselect_b32 s3, 0, 0
	v_lshlrev_b64 v[2:3], 7, v[2:3]
	v_add_u32_e32 v4, s15, v1
	s_add_i32 s22, s2, s3
	v_lshlrev_b32_e32 v1, 4, v6
	s_lshr_b32 s3, s17, 1
	v_lshl_add_u64 v[2:3], s[4:5], 0, v[2:3]
	v_ashrrev_i32_e32 v5, 31, v4
	v_and_b32_e32 v96, 0x70, v1
	s_add_i32 s24, s22, 0x8000
	s_and_b32 s20, s3, 0x7fffffc0
	v_lshlrev_b64 v[4:5], 7, v[4:5]
	v_lshl_add_u64 v[104:105], v[2:3], 0, v[96:97]
	s_bitcmp1_b32 s17, 6
	s_mov_b64 s[4:5], 0x2000
	s_mov_b32 m0, s22
	s_nop 0
	global_load_lds_dwordx4 v[104:105], off
	v_lshl_add_u64 v[4:5], s[6:7], 0, v[4:5]
	s_cselect_b32 s16, 0x60, 0
	v_lshl_add_u64 v[110:111], v[104:105], 0, s[4:5]
	s_mov_b64 s[6:7], 0x4000
	s_add_i32 s3, s22, 0x2000
	s_mov_b32 m0, s3
	s_nop 0
	global_load_lds_dwordx4 v[110:111], off
	v_lshl_add_u64 v[108:109], v[104:105], 0, s[6:7]
	s_mov_b64 s[26:27], 0x6000
	s_add_i32 s3, s22, 0x4000
	s_mov_b32 m0, s3
	s_nop 0
	global_load_lds_dwordx4 v[108:109], off
	v_lshl_add_u64 v[106:107], v[104:105], 0, s[26:27]
	s_add_i32 s3, s22, 0x6000
	s_mov_b32 m0, s3
	s_nop 0
	global_load_lds_dwordx4 v[106:107], off
	v_lshl_add_u64 v[98:99], v[4:5], 0, v[96:97]
	s_mov_b32 m0, s24
	s_nop 0
	global_load_lds_dwordx4 v[98:99], off
	v_lshl_add_u64 v[100:101], v[98:99], 0, s[4:5]
	s_add_i32 s3, s22, 0xa000
	s_mov_b32 m0, s3
	s_nop 0
	global_load_lds_dwordx4 v[100:101], off
	v_lshl_add_u64 v[102:103], v[98:99], 0, s[6:7]
	s_add_i32 s3, s22, 0xc000
	s_mov_b32 m0, s3
	s_nop 0
	global_load_lds_dwordx4 v[102:103], off
	s_mov_b32 s21, 1
	s_mov_b32 s23, 0
	s_cmp_lt_i32 s10, 64
	v_mov_b32_e32 v96, v97
	v_mov_b32_e32 v95, v97
	v_mov_b32_e32 v94, v97
	v_mov_b32_e32 v93, v97
	v_mov_b32_e32 v92, v97
	v_mov_b32_e32 v91, v97
	v_mov_b32_e32 v90, v97
	v_mov_b32_e32 v89, v97
	v_mov_b32_e32 v88, v97
	v_mov_b32_e32 v87, v97
	v_mov_b32_e32 v86, v97
	v_mov_b32_e32 v85, v97
	v_mov_b32_e32 v84, v97
	v_mov_b32_e32 v83, v97
	v_mov_b32_e32 v82, v97
	v_mov_b32_e32 v81, v97
	v_mov_b32_e32 v80, v97
	v_mov_b32_e32 v79, v97
	v_mov_b32_e32 v78, v97
	v_mov_b32_e32 v77, v97
	v_mov_b32_e32 v76, v97
	v_mov_b32_e32 v75, v97
	v_mov_b32_e32 v74, v97
	v_mov_b32_e32 v73, v97
	v_mov_b32_e32 v72, v97
	v_mov_b32_e32 v71, v97
	v_mov_b32_e32 v70, v97
	v_mov_b32_e32 v69, v97
	v_mov_b32_e32 v68, v97
	v_mov_b32_e32 v67, v97
	v_mov_b32_e32 v66, v97
	v_mov_b32_e32 v65, v97
	v_mov_b32_e32 v64, v97
	v_mov_b32_e32 v63, v97
	v_mov_b32_e32 v62, v97
	v_mov_b32_e32 v61, v97
	v_mov_b32_e32 v60, v97
	v_mov_b32_e32 v59, v97
	v_mov_b32_e32 v58, v97
	v_mov_b32_e32 v57, v97
	v_mov_b32_e32 v56, v97
	v_mov_b32_e32 v55, v97
	v_mov_b32_e32 v54, v97
	v_mov_b32_e32 v53, v97
	v_mov_b32_e32 v52, v97
	v_mov_b32_e32 v51, v97
	v_mov_b32_e32 v50, v97
	v_mov_b32_e32 v49, v97
	v_mov_b32_e32 v48, v97
	v_mov_b32_e32 v47, v97
	v_mov_b32_e32 v46, v97
	v_mov_b32_e32 v45, v97
	v_mov_b32_e32 v44, v97
	v_mov_b32_e32 v43, v97
	v_mov_b32_e32 v42, v97
	v_mov_b32_e32 v41, v97
	v_mov_b32_e32 v40, v97
	v_mov_b32_e32 v39, v97
	v_mov_b32_e32 v38, v97
	v_mov_b32_e32 v37, v97
	v_mov_b32_e32 v36, v97
	v_mov_b32_e32 v35, v97
	v_mov_b32_e32 v34, v97
	v_mov_b32_e32 v33, v97
	v_mov_b32_e32 v32, v97
	v_mov_b32_e32 v31, v97
	v_mov_b32_e32 v30, v97
	v_mov_b32_e32 v29, v97
	v_mov_b32_e32 v28, v97
	v_mov_b32_e32 v27, v97
	v_mov_b32_e32 v26, v97
	v_mov_b32_e32 v25, v97
	v_mov_b32_e32 v24, v97
	v_mov_b32_e32 v23, v97
	v_mov_b32_e32 v22, v97
	v_mov_b32_e32 v21, v97
	v_mov_b32_e32 v20, v97
	v_mov_b32_e32 v19, v97
	v_mov_b32_e32 v18, v97
	v_mov_b32_e32 v17, v97
	v_mov_b32_e32 v16, v97
	v_mov_b32_e32 v15, v97
	v_mov_b32_e32 v14, v97
	v_mov_b32_e32 v13, v97
	v_mov_b32_e32 v12, v97
	v_mov_b32_e32 v11, v97
	v_mov_b32_e32 v10, v97
	v_mov_b32_e32 v9, v97
	v_mov_b32_e32 v8, v97
	v_mov_b32_e32 v7, v97
	v_mov_b32_e32 v6, v97
	v_mov_b32_e32 v5, v97
	v_mov_b32_e32 v4, v97
	v_mov_b32_e32 v3, v97
	v_mov_b32_e32 v2, v97
	v_and_b32_e32 v162, 31, v0
	v_bfe_u32 v1, v0, 5, 1
	s_cbranch_scc1 .LBB2_6
	s_ashr_i32 s3, s10, 31
	s_lshr_b32 s3, s3, 26
	s_add_i32 s3, s10, s3
	v_lshrrev_b32_e32 v2, 1, v0
	s_ashr_i32 s25, s3, 6
	v_bitop3_b32 v2, v1, v2, 7 bitop3:0x78
	s_cmp_lg_u32 0, -1
	v_lshlrev_b32_e32 v120, 4, v2
	v_or_b32_e32 v2, s20, v162
	s_cselect_b32 s3, 0, 0
	v_lshl_add_u32 v121, v2, 7, 0
	v_or_b32_e32 v2, s16, v162
	s_mov_b32 s10, s8
	s_add_i32 s8, s3, s2
	s_ashr_i32 s3, s9, 31
	s_mov_b32 s2, s9
	v_lshl_add_u32 v122, v2, 7, 0
	s_lshl_b64 s[2:3], s[2:3], 7
	v_mov_b32_e32 v2, 0
	s_addk_i32 s8, 0x6000
	v_xor_b32_e32 v123, 32, v120
	v_xor_b32_e32 v124, 64, v120
	v_xor_b32_e32 v125, 0x60, v120
	s_lshl_b64 s[4:5], s[10:11], 7
	s_mov_b64 s[6:7], s[2:3]
	s_mov_b32 s9, 0
	v_mov_b32_e32 v3, v2
	v_mov_b32_e32 v4, v2
	v_mov_b32_e32 v5, v2
	v_mov_b32_e32 v6, v2
	v_mov_b32_e32 v7, v2
	v_mov_b32_e32 v8, v2
	v_mov_b32_e32 v9, v2
	v_mov_b32_e32 v10, v2
	v_mov_b32_e32 v11, v2
	v_mov_b32_e32 v12, v2
	v_mov_b32_e32 v13, v2
	v_mov_b32_e32 v14, v2
	v_mov_b32_e32 v15, v2
	v_mov_b32_e32 v16, v2
	v_mov_b32_e32 v17, v2
	v_mov_b32_e32 v18, v2
	v_mov_b32_e32 v19, v2
	v_mov_b32_e32 v20, v2
	v_mov_b32_e32 v21, v2
	v_mov_b32_e32 v22, v2
	v_mov_b32_e32 v23, v2
	v_mov_b32_e32 v24, v2
	v_mov_b32_e32 v25, v2
	v_mov_b32_e32 v26, v2
	v_mov_b32_e32 v27, v2
	v_mov_b32_e32 v28, v2
	v_mov_b32_e32 v29, v2
	v_mov_b32_e32 v30, v2
	v_mov_b32_e32 v31, v2
	v_mov_b32_e32 v32, v2
	v_mov_b32_e32 v33, v2
	v_mov_b32_e32 v34, v2
	v_mov_b32_e32 v35, v2
	v_mov_b32_e32 v36, v2
	v_mov_b32_e32 v37, v2
	v_mov_b32_e32 v38, v2
	v_mov_b32_e32 v39, v2
	v_mov_b32_e32 v40, v2
	v_mov_b32_e32 v41, v2
	v_mov_b32_e32 v42, v2
	v_mov_b32_e32 v43, v2
	v_mov_b32_e32 v44, v2
	v_mov_b32_e32 v45, v2
	v_mov_b32_e32 v46, v2
	v_mov_b32_e32 v47, v2
	v_mov_b32_e32 v48, v2
	v_mov_b32_e32 v49, v2
	v_mov_b32_e32 v50, v2
	v_mov_b32_e32 v51, v2
	v_mov_b32_e32 v52, v2
	v_mov_b32_e32 v53, v2
	v_mov_b32_e32 v54, v2
	v_mov_b32_e32 v55, v2
	v_mov_b32_e32 v56, v2
	v_mov_b32_e32 v57, v2
	v_mov_b32_e32 v58, v2
	v_mov_b32_e32 v59, v2
	v_mov_b32_e32 v60, v2
	v_mov_b32_e32 v61, v2
	v_mov_b32_e32 v62, v2
	v_mov_b32_e32 v63, v2
	v_mov_b32_e32 v64, v2
	v_mov_b32_e32 v65, v2
	v_mov_b32_e32 v66, v2
	v_mov_b32_e32 v67, v2
	v_mov_b32_e32 v68, v2
	v_mov_b32_e32 v69, v2
	v_mov_b32_e32 v70, v2
	v_mov_b32_e32 v71, v2
	v_mov_b32_e32 v72, v2
	v_mov_b32_e32 v73, v2
	v_mov_b32_e32 v74, v2
	v_mov_b32_e32 v75, v2
	v_mov_b32_e32 v76, v2
	v_mov_b32_e32 v77, v2
	v_mov_b32_e32 v78, v2
	v_mov_b32_e32 v79, v2
	v_mov_b32_e32 v80, v2
	v_mov_b32_e32 v81, v2
	v_mov_b32_e32 v82, v2
	v_mov_b32_e32 v83, v2
	v_mov_b32_e32 v84, v2
	v_mov_b32_e32 v85, v2
	v_mov_b32_e32 v86, v2
	v_mov_b32_e32 v87, v2
	v_mov_b32_e32 v88, v2
	v_mov_b32_e32 v89, v2
	v_mov_b32_e32 v90, v2
	v_mov_b32_e32 v91, v2
	v_mov_b32_e32 v92, v2
	v_mov_b32_e32 v93, v2
	v_mov_b32_e32 v94, v2
	v_mov_b32_e32 v95, v2
	v_mov_b32_e32 v96, v2
	v_mov_b32_e32 v97, v2
	v_lshl_add_u64 v[168:169], v[104:105], 0, s[4:5]
	v_lshl_add_u64 v[170:171], v[110:111], 0, s[4:5]
	v_lshl_add_u64 v[172:173], v[108:109], 0, s[4:5]
	v_lshl_add_u64 v[174:175], v[106:107], 0, s[4:5]
	v_lshl_add_u64 v[176:177], v[98:99], 0, s[2:3]
	v_lshl_add_u64 v[178:179], v[100:101], 0, s[2:3]
	v_lshl_add_u64 v[180:181], v[102:103], 0, s[2:3]
	s_mov_b32 s9, 1
	s_add_i32 s25, s25, -1
	s_add_i32 s11, s22, 0xe000
	s_mov_b32 m0, s11
	s_nop 0
	global_load_lds_dwordx4 v[168:169], off
	v_lshl_add_u64 v[168:169], v[168:169], 0, s[4:5]
	s_add_i32 m0, s11, 0x2000
	s_nop 0
	global_load_lds_dwordx4 v[170:171], off
	v_lshl_add_u64 v[170:171], v[170:171], 0, s[4:5]
	s_add_i32 m0, s11, 0x4000
	s_nop 0
	global_load_lds_dwordx4 v[172:173], off
	v_lshl_add_u64 v[172:173], v[172:173], 0, s[4:5]
	s_add_i32 m0, s11, 0x6000
	s_nop 0
	global_load_lds_dwordx4 v[174:175], off
	v_lshl_add_u64 v[174:175], v[174:175], 0, s[4:5]
	s_add_i32 m0, s11, 0x8000
	s_nop 0
	global_load_lds_dwordx4 v[176:177], off
	v_lshl_add_u64 v[176:177], v[176:177], 0, s[2:3]
	s_add_i32 m0, s11, 0xa000
	s_nop 0
	global_load_lds_dwordx4 v[178:179], off
	v_lshl_add_u64 v[178:179], v[178:179], 0, s[2:3]
	s_add_i32 m0, s11, 0xc000
	s_nop 0
	global_load_lds_dwordx4 v[180:181], off
	v_lshl_add_u64 v[180:181], v[180:181], 0, s[2:3]
	s_cmp_ge_u32 s14, 4
	s_cbranch_scc1 .Lqkv_a0
	s_waitcnt vmcnt(7) lgkmcnt(0)
	s_barrier
	s_mul_i32 s10, s23, 0xe000
	v_add_u32_e32 v142, s10, v122
	v_add_u32_e32 v143, s10, v121
	s_xor_b32 s23, s23, 1
	s_xor_b32 s21, s21, 1
	v_add_u32_e32 v144, v142, v120
	v_add_u32_e32 v145, v143, v120
	ds_read_b128 v[130:133], v145
	ds_read_b128 v[104:107], v144 offset:32768
	ds_read_b128 v[108:111], v144 offset:36864
	ds_read_b128 v[134:137], v145 offset:4096
	ds_read_b128 v[126:129], v144 offset:40960
	v_add_u32_e32 v146, v142, v123
	v_add_u32_e32 v147, v143, v123
	ds_read_b128 v[182:185], v147
	ds_read_b128 v[138:141], v146 offset:32768
	ds_read_b128 v[112:115], v146 offset:36864
	ds_read_b128 v[186:189], v147 offset:4096
	ds_read_b128 v[116:119], v146 offset:40960
	s_waitcnt lgkmcnt(8)
	v_mfma_f32_32x32x16_f16 v[82:97], v[104:107], v[130:133], v[82:97]
	s_waitcnt lgkmcnt(7)
	v_mfma_f32_32x32x16_f16 v[66:81], v[108:111], v[130:133], v[66:81]
	s_waitcnt lgkmcnt(6)
	v_mfma_f32_32x32x16_f16 v[34:49], v[104:107], v[134:137], v[34:49]
	v_mfma_f32_32x32x16_f16 v[18:33], v[108:111], v[134:137], v[18:33]
	s_waitcnt lgkmcnt(5)
	v_mfma_f32_32x32x16_f16 v[50:65], v[126:129], v[130:133], v[50:65]
	v_mfma_f32_32x32x16_f16 v[2:17], v[126:129], v[134:137], v[2:17]
	v_add_u32_e32 v144, v142, v124
	v_add_u32_e32 v145, v143, v124
	ds_read_b128 v[130:133], v145
	ds_read_b128 v[104:107], v144 offset:32768
	ds_read_b128 v[108:111], v144 offset:36864
	ds_read_b128 v[134:137], v145 offset:4096
	ds_read_b128 v[126:129], v144 offset:40960
	s_waitcnt lgkmcnt(8)
	v_mfma_f32_32x32x16_f16 v[82:97], v[138:141], v[182:185], v[82:97]
	s_waitcnt lgkmcnt(7)
	v_mfma_f32_32x32x16_f16 v[66:81], v[112:115], v[182:185], v[66:81]
	s_waitcnt lgkmcnt(6)
	v_mfma_f32_32x32x16_f16 v[34:49], v[138:141], v[186:189], v[34:49]
	v_mfma_f32_32x32x16_f16 v[18:33], v[112:115], v[186:189], v[18:33]
	s_waitcnt lgkmcnt(5)
	v_mfma_f32_32x32x16_f16 v[50:65], v[116:119], v[182:185], v[50:65]
	v_mfma_f32_32x32x16_f16 v[2:17], v[116:119], v[186:189], v[2:17]
	v_add_u32_e32 v146, v142, v125
	v_add_u32_e32 v147, v143, v125
	ds_read_b128 v[182:185], v147
	ds_read_b128 v[138:141], v146 offset:32768
	ds_read_b128 v[112:115], v146 offset:36864
	ds_read_b128 v[186:189], v147 offset:4096
	ds_read_b128 v[116:119], v146 offset:40960
	s_waitcnt lgkmcnt(8)
	v_mfma_f32_32x32x16_f16 v[82:97], v[104:107], v[130:133], v[82:97]
	s_waitcnt lgkmcnt(7)
	v_mfma_f32_32x32x16_f16 v[66:81], v[108:111], v[130:133], v[66:81]
	s_waitcnt lgkmcnt(6)
	v_mfma_f32_32x32x16_f16 v[34:49], v[104:107], v[134:137], v[34:49]
	v_mfma_f32_32x32x16_f16 v[18:33], v[108:111], v[134:137], v[18:33]
	s_waitcnt lgkmcnt(5)
	v_mfma_f32_32x32x16_f16 v[50:65], v[126:129], v[130:133], v[50:65]
	v_mfma_f32_32x32x16_f16 v[2:17], v[126:129], v[134:137], v[2:17]

.Lqkv_a0:
	s_waitcnt vmcnt(7)
	s_barrier
	s_mul_i32 s10, s23, 0xe000
	v_add_u32_e32 v142, s10, v122
	v_add_u32_e32 v143, s10, v121
	s_xor_b32 s23, s23, 1
	s_xor_b32 s21, s21, 1
	v_add_u32_e32 v144, v142, v120
	v_add_u32_e32 v145, v143, v120
	ds_read_b128 v[130:133], v145
	ds_read_b128 v[104:107], v144 offset:32768
	ds_read_b128 v[108:111], v144 offset:36864
	ds_read_b128 v[134:137], v145 offset:4096
	ds_read_b128 v[126:129], v144 offset:40960
	v_add_u32_e32 v146, v142, v123
	v_add_u32_e32 v147, v143, v123
	ds_read_b128 v[182:185], v147
	ds_read_b128 v[138:141], v146 offset:32768
	ds_read_b128 v[112:115], v146 offset:36864
	ds_read_b128 v[186:189], v147 offset:4096
	ds_read_b128 v[116:119], v146 offset:40960
	s_waitcnt lgkmcnt(8)
	v_mfma_f32_32x32x16_f16 v[82:97], v[104:107], v[130:133], v[82:97]
	s_waitcnt lgkmcnt(7)
	v_mfma_f32_32x32x16_f16 v[66:81], v[108:111], v[130:133], v[66:81]
	s_waitcnt lgkmcnt(6)
	v_mfma_f32_32x32x16_f16 v[34:49], v[104:107], v[134:137], v[34:49]
	v_mfma_f32_32x32x16_f16 v[18:33], v[108:111], v[134:137], v[18:33]
	s_waitcnt lgkmcnt(5)
	v_mfma_f32_32x32x16_f16 v[50:65], v[126:129], v[130:133], v[50:65]
	v_mfma_f32_32x32x16_f16 v[2:17], v[126:129], v[134:137], v[2:17]
	v_add_u32_e32 v144, v142, v124
	v_add_u32_e32 v145, v143, v124
	ds_read_b128 v[130:133], v145
	ds_read_b128 v[104:107], v144 offset:32768
	ds_read_b128 v[108:111], v144 offset:36864
	ds_read_b128 v[134:137], v145 offset:4096
	ds_read_b128 v[126:129], v144 offset:40960
	s_waitcnt lgkmcnt(8)
	v_mfma_f32_32x32x16_f16 v[82:97], v[138:141], v[182:185], v[82:97]
	s_waitcnt lgkmcnt(7)
	v_mfma_f32_32x32x16_f16 v[66:81], v[112:115], v[182:185], v[66:81]
	s_waitcnt lgkmcnt(6)
	v_mfma_f32_32x32x16_f16 v[34:49], v[138:141], v[186:189], v[34:49]
	v_mfma_f32_32x32x16_f16 v[18:33], v[112:115], v[186:189], v[18:33]
	s_waitcnt lgkmcnt(5)
	v_mfma_f32_32x32x16_f16 v[50:65], v[116:119], v[182:185], v[50:65]
	v_mfma_f32_32x32x16_f16 v[2:17], v[116:119], v[186:189], v[2:17]
	v_add_u32_e32 v146, v142, v125
	v_add_u32_e32 v147, v143, v125
	ds_read_b128 v[182:185], v147
	ds_read_b128 v[138:141], v146 offset:32768
	ds_read_b128 v[112:115], v146 offset:36864
	ds_read_b128 v[186:189], v147 offset:4096
	ds_read_b128 v[116:119], v146 offset:40960
	s_waitcnt lgkmcnt(8)
	v_mfma_f32_32x32x16_f16 v[82:97], v[104:107], v[130:133], v[82:97]
	s_waitcnt lgkmcnt(7)
	v_mfma_f32_32x32x16_f16 v[66:81], v[108:111], v[130:133], v[66:81]
	s_waitcnt lgkmcnt(6)
	v_mfma_f32_32x32x16_f16 v[34:49], v[104:107], v[134:137], v[34:49]
	v_mfma_f32_32x32x16_f16 v[18:33], v[108:111], v[134:137], v[18:33]
	s_waitcnt lgkmcnt(5)
	v_mfma_f32_32x32x16_f16 v[50:65], v[126:129], v[130:133], v[50:65]
	v_mfma_f32_32x32x16_f16 v[2:17], v[126:129], v[134:137], v[2:17]
	s_waitcnt lgkmcnt(3)
	v_mfma_f32_32x32x16_f16 v[82:97], v[138:141], v[182:185], v[82:97]
	s_waitcnt lgkmcnt(2)
	v_mfma_f32_32x32x16_f16 v[66:81], v[112:115], v[182:185], v[66:81]
	s_waitcnt lgkmcnt(1)
	v_mfma_f32_32x32x16_f16 v[34:49], v[138:141], v[186:189], v[34:49]
	v_mfma_f32_32x32x16_f16 v[18:33], v[112:115], v[186:189], v[18:33]
	s_waitcnt lgkmcnt(0)
	v_mfma_f32_32x32x16_f16 v[50:65], v[116:119], v[182:185], v[50:65]
	v_mfma_f32_32x32x16_f16 v[2:17], v[116:119], v[186:189], v[2:17]
